# SB step: key-index adds and strict-causal compares (64 VALU) moved into the diagonal-tile-only block
# speedup vs baseline: 1.0114x; 1.0026x over previous
; #define LAS __attribute__((address_space(3)))
; __device__ __forceinline__ float ex2(float x) { return __builtin_amdgcn_exp2f(x); }
; __device__ __forceinline__ float lg2(float x) { return __builtin_amdgcn_logf(x); }
; __device__ __forceinline__ f32x16 mfma32(bf16x8 a, bf16x8 b, f32x16 c) { return __builtin_amdgcn_mfma_f32_32x32x16_bf16(a, b, c, 0, 0, 0); }
; #define SB_DMA(t, s) do { glds(ksrc + (size_t)(t) * 64 * INP, shm + (s) * KS_SB + wid * 1024); glds(vsrc + (size_t)(t) * 64 * INP, shm + SB_VOFF + (s) * VS + wid * 1024); } while (0)
; #define SB_WAITBAR() asm volatile("s_waitcnt vmcnt(4) lgkmcnt(0)\n\ts_barrier" ::: "memory")
; __device__ __forceinline__ void sb_unit(int b, int h, int qb, const bf16_t* __restrict__ PROJ, bf16_t* OCAT, float* SSQO, ldsp shm, volatile LAS unsigned* FL) {
;     ...
;         SB_WAITBAR();
;         if (step > 0) { if (FL[(step - 1) % 3] == 0xFFu) break; }
;         if (tid == 0) FL[(step + 1) % 3] = 0u;
;         SB_DMA(SB_TILE(step + 3), (step + 3) & 3);
;         if (t <= tdw && !wfin) {
;             const LAS unsigned char* kb = shm + (step & 3) * KS_SB + hi * 1024 + r32 * 16;
;             f32x16 z0 = f32x16{}, z1 = f32x16{};
; #pragma unroll
;             for (int d0 = 0; d0 < 4; ++d0) { const bf16x8 k0 = *(const LAS bf16x8*)(kb + d0 * 2048), k1 = *(const LAS bf16x8*)(kb + d0 * 2048 + 512);
;                 z0 = mfma32(k0, qr[d0], z0); z1 = mfma32(k1, qr[d0], z1); }
;             const bool diag = (t == tdw); const int kb0 = t * 64 + 4 * hi;
;             f32x16 l0, l1; float tot = 0.f;
; #pragma unroll
;             for (int r = 0; r < 16; ++r) { l0[r] = -lg2(1.0f + ex2(fminf(z0[r], 100.f))); l1[r] = -lg2(1.0f + ex2(fminf(z1[r], 100.f))); }
.LBB0_1055:
	s_or_b64 exec, exec, s[4:5]
	s_add_i32 s6, s34, s2
	s_max_i32 s8, s6, 0
	s_add_i32 s7, s3, 0x6000
	s_lshl_b64 s[4:5], s[8:9], 18
	s_and_b32 s7, s7, 0x6000
	v_lshl_add_u64 v[38:39], v[154:155], 0, s[4:5]
	s_add_i32 s7, s26, s7
	v_lshl_add_u64 v[38:39], v[38:39], 0, s[82:83]
	s_mov_b32 m0, s7
	s_add_i32 s6, s6, 3
	global_load_lds_dwordx4 v[38:39], off
	v_lshl_add_u64 v[38:39], v[156:157], 0, s[4:5]
	v_lshl_add_u64 v[38:39], v[38:39], 0, s[84:85]
	s_add_i32 m0, s7, 0x8000
	s_cmp_gt_i32 s6, s35
	global_load_lds_dwordx4 v[38:39], off
	s_cselect_b64 s[4:5], -1, 0
	s_or_b64 s[4:5], s[0:1], s[4:5]
	s_and_b64 vcc, exec, s[4:5]
	s_cbranch_vccnz .LBB0_1061
	s_and_b32 s8, s3, 0x6000
	v_add_u32_e32 v1, s8, v164
	ds_read_b128 v[38:41], v1
	ds_read_b128 v[42:45], v1 offset:512
	s_cmp_eq_u32 s27, s2
	s_cselect_b64 s[16:17], -1, 0
	s_cmp_lg_u32 s27, s2
	s_waitcnt lgkmcnt(0)
	v_mfma_f32_32x32x16_bf16 v[98:113], v[38:41], v[130:133], 0
	v_mfma_f32_32x32x16_bf16 v[82:97], v[42:45], v[130:133], 0
	ds_read_b128 v[38:41], v1 offset:2048
	ds_read_b128 v[42:45], v1 offset:2560
	s_waitcnt lgkmcnt(0)
	v_mfma_f32_32x32x16_bf16 v[82:97], v[42:45], v[134:137], v[82:97]
	v_mfma_f32_32x32x16_bf16 v[98:113], v[38:41], v[134:137], v[98:113]
	ds_read_b128 v[38:41], v1 offset:4096
	ds_read_b128 v[42:45], v1 offset:4608
	s_waitcnt lgkmcnt(0)
	v_mfma_f32_32x32x16_bf16 v[82:97], v[42:45], v[138:141], v[82:97]
	v_mfma_f32_32x32x16_bf16 v[98:113], v[38:41], v[138:141], v[98:113]
	ds_read_b128 v[38:41], v1 offset:6144
	ds_read_b128 v[42:45], v1 offset:6656
	s_waitcnt lgkmcnt(0)
	v_mfma_f32_32x32x16_bf16 v[82:97], v[42:45], v[142:145], v[82:97]
	v_mfma_f32_32x32x16_bf16 v[98:113], v[38:41], v[142:145], v[98:113]
	s_nop 10
	v_min_f32_e32 v2, 0x42c80000, v82
	v_exp_f32_e32 v2, v2
	v_min_f32_e32 v60, 0x42c80000, v94
	v_exp_f32_e32 v60, v60
	v_add_f32_e32 v2, 1.0, v2
	v_min_f32_e32 v37, 0x42c80000, v99
	v_exp_f32_e32 v37, v37
	v_min_f32_e32 v1, 0x42c80000, v98
	v_exp_f32_e32 v1, v1
	v_log_f32_e32 v38, v2
	v_add_f32_e32 v2, 1.0, v37
	v_log_f32_e32 v37, v2
	v_add_f32_e32 v1, 1.0, v1
	v_min_f32_e32 v2, 0x42c80000, v83
	v_log_f32_e32 v1, v1
	v_exp_f32_e32 v39, v2
	v_xor_b32_e32 v52, 0x80000000, v38
	v_xor_b32_e32 v2, 0x80000000, v1
	v_xor_b32_e32 v1, 0x80000000, v37
	v_add_f32_e32 v37, 1.0, v39
	v_min_f32_e32 v38, 0x42c80000, v100
	v_min_f32_e32 v39, 0x42c80000, v84
	v_exp_f32_e32 v38, v38
	v_exp_f32_e32 v39, v39
	v_min_f32_e32 v59, 0x42c80000, v110
	v_exp_f32_e32 v59, v59
	v_add_f32_e32 v38, 1.0, v38
	v_add_f32_e32 v39, 1.0, v39
	v_log_f32_e32 v38, v38
	v_log_f32_e32 v39, v39
	v_add_f32_e32 v59, 1.0, v59
	v_log_f32_e32 v74, v59
	v_add_f32_e32 v59, 1.0, v60
	v_min_f32_e32 v60, 0x42c80000, v111
	v_min_f32_e32 v40, 0x42c80000, v101
	v_xor_b32_e32 v54, 0x80000000, v38
	v_xor_b32_e32 v56, 0x80000000, v39
	v_exp_f32_e32 v60, v60
	v_min_f32_e32 v61, 0x42c80000, v95
	v_log_f32_e32 v37, v37
	v_exp_f32_e32 v40, v40
	v_min_f32_e32 v38, 0x42c80000, v85
	v_min_f32_e32 v39, 0x42c80000, v102
	v_exp_f32_e32 v61, v61
	v_exp_f32_e32 v38, v38
	v_exp_f32_e32 v39, v39
	v_log_f32_e32 v75, v59
	v_add_f32_e32 v59, 1.0, v60
	v_xor_b32_e32 v53, 0x80000000, v37
	v_add_f32_e32 v37, 1.0, v40
	v_log_f32_e32 v77, v59
	v_add_f32_e32 v59, 1.0, v61
	v_min_f32_e32 v60, 0x42c80000, v112
	v_add_f32_e32 v38, 1.0, v38
	v_add_f32_e32 v39, 1.0, v39
	v_min_f32_e32 v40, 0x42c80000, v86
	v_exp_f32_e32 v60, v60
	v_min_f32_e32 v61, 0x42c80000, v96
	v_log_f32_e32 v37, v37
	v_log_f32_e32 v38, v38
	v_log_f32_e32 v39, v39
	v_exp_f32_e32 v40, v40
	v_exp_f32_e32 v61, v61
	v_log_f32_e32 v78, v59
	v_add_f32_e32 v59, 1.0, v60
	v_xor_b32_e32 v55, 0x80000000, v37
	v_xor_b32_e32 v57, 0x80000000, v38
	v_xor_b32_e32 v58, 0x80000000, v39
	v_add_f32_e32 v37, 1.0, v40
	v_log_f32_e32 v79, v59
	v_add_f32_e32 v59, 1.0, v61
	v_min_f32_e32 v60, 0x42c80000, v113
	v_min_f32_e32 v38, 0x42c80000, v103
	v_min_f32_e32 v39, 0x42c80000, v87
	v_min_f32_e32 v40, 0x42c80000, v104
	v_min_f32_e32 v41, 0x42c80000, v88
	v_min_f32_e32 v42, 0x42c80000, v105
	v_min_f32_e32 v43, 0x42c80000, v89
	v_min_f32_e32 v44, 0x42c80000, v106
	v_min_f32_e32 v45, 0x42c80000, v90
	v_min_f32_e32 v46, 0x42c80000, v107
	v_min_f32_e32 v47, 0x42c80000, v91
	v_min_f32_e32 v48, 0x42c80000, v108
	v_min_f32_e32 v49, 0x42c80000, v92
	v_min_f32_e32 v50, 0x42c80000, v109
	v_min_f32_e32 v51, 0x42c80000, v93
	v_exp_f32_e32 v60, v60
	v_min_f32_e32 v61, 0x42c80000, v97
	v_exp_f32_e32 v38, v38
	v_exp_f32_e32 v39, v39
	v_exp_f32_e32 v40, v40
	v_exp_f32_e32 v41, v41
	v_exp_f32_e32 v42, v42
	v_exp_f32_e32 v43, v43
	v_exp_f32_e32 v44, v44
	v_exp_f32_e32 v45, v45
	v_exp_f32_e32 v46, v46
	v_exp_f32_e32 v47, v47
	v_exp_f32_e32 v48, v48
	v_exp_f32_e32 v49, v49
	v_exp_f32_e32 v50, v50
	v_exp_f32_e32 v51, v51
	v_exp_f32_e32 v61, v61
	v_log_f32_e32 v80, v59
	v_add_f32_e32 v59, 1.0, v60
	v_add_f32_e32 v38, 1.0, v38
	v_add_f32_e32 v39, 1.0, v39
	v_add_f32_e32 v40, 1.0, v40
	v_add_f32_e32 v41, 1.0, v41
	v_add_f32_e32 v42, 1.0, v42
	v_add_f32_e32 v43, 1.0, v43
	v_add_f32_e32 v44, 1.0, v44
	v_add_f32_e32 v45, 1.0, v45
	v_add_f32_e32 v46, 1.0, v46
	v_add_f32_e32 v47, 1.0, v47
	v_add_f32_e32 v48, 1.0, v48
	v_add_f32_e32 v49, 1.0, v49
	v_add_f32_e32 v50, 1.0, v50
	v_add_f32_e32 v51, 1.0, v51
	v_log_f32_e32 v81, v59
	v_add_f32_e32 v59, 1.0, v61
	v_log_f32_e32 v37, v37
	v_log_f32_e32 v38, v38
	v_log_f32_e32 v39, v39
	v_log_f32_e32 v40, v40
	v_log_f32_e32 v41, v41
	v_log_f32_e32 v42, v42
	v_log_f32_e32 v43, v43
	v_log_f32_e32 v44, v44
	v_log_f32_e32 v45, v45
	v_log_f32_e32 v46, v46
	v_log_f32_e32 v47, v47
	v_log_f32_e32 v48, v48
	v_log_f32_e32 v49, v49
	v_log_f32_e32 v50, v50
	v_log_f32_e32 v51, v51
	v_log_f32_e32 v114, v59
	v_xor_b32_e32 v60, 0x80000000, v37
	v_xor_b32_e32 v59, 0x80000000, v38
	v_xor_b32_e32 v61, 0x80000000, v39
	v_xor_b32_e32 v62, 0x80000000, v40
	v_xor_b32_e32 v64, 0x80000000, v41
	v_xor_b32_e32 v63, 0x80000000, v42
	v_xor_b32_e32 v65, 0x80000000, v43
	v_xor_b32_e32 v66, 0x80000000, v44
	v_xor_b32_e32 v68, 0x80000000, v45
	v_xor_b32_e32 v67, 0x80000000, v46
	v_xor_b32_e32 v69, 0x80000000, v47
	v_xor_b32_e32 v70, 0x80000000, v48
	v_xor_b32_e32 v72, 0x80000000, v49
	v_xor_b32_e32 v71, 0x80000000, v50
	v_xor_b32_e32 v73, 0x80000000, v51
	v_xor_b32_e32 v74, 0x80000000, v74
	v_xor_b32_e32 v76, 0x80000000, v75
	v_xor_b32_e32 v75, 0x80000000, v77
	v_xor_b32_e32 v77, 0x80000000, v78
	v_xor_b32_e32 v78, 0x80000000, v79
	v_xor_b32_e32 v80, 0x80000000, v80
	v_xor_b32_e32 v79, 0x80000000, v81
	v_xor_b32_e32 v81, 0x80000000, v114
	s_cbranch_scc1 .LBB0_1058
; __device__ __forceinline__ float ex2(float x) { return __builtin_amdgcn_exp2f(x); }
; __device__ __forceinline__ float lg2(float x) { return __builtin_amdgcn_logf(x); }
; __device__ __forceinline__ void sb_unit(int b, int h, int qb, const bf16_t* __restrict__ PROJ, bf16_t* OCAT, float* SSQO, ldsp shm, volatile LAS unsigned* FL) {
;     ...
;             const bool diag = (t == tdw); const int kb0 = t * 64 + 4 * hi;
;             f32x16 l0, l1; float tot = 0.f;
; #pragma unroll
;             for (int r = 0; r < 16; ++r) { l0[r] = -lg2(1.0f + ex2(fminf(z0[r], 100.f))); l1[r] = -lg2(1.0f + ex2(fminf(z1[r], 100.f))); }
;             if (diag) {
; #pragma unroll
;                 for (int r = 0; r < 16; ++r) { const int kk = kb0 + (r & 3) + 8 * (r >> 2); if (kk >= qabs) l0[r] = 0.f; if (kk + 32 >= qabs) l1[r] = 0.f; } }
	v_add_u32_e32 v166, s33, v165
	v_add_u32_e32 v167, 0xc0, v166
	v_add_u32_e32 v168, 0xe0, v166
	v_add_u32_e32 v169, 0xc1, v166
	v_add_u32_e32 v170, 0xe1, v166
	v_add_u32_e32 v171, 0xc2, v166
	v_add_u32_e32 v172, 0xe2, v166
	v_add_u32_e32 v173, 0xc3, v166
	v_add_u32_e32 v174, 0xe3, v166
	v_add_u32_e32 v175, 0xc8, v166
	v_add_u32_e32 v176, 0xe8, v166
	v_add_u32_e32 v177, 0xc9, v166
	v_add_u32_e32 v178, 0xe9, v166
	v_add_u32_e32 v179, 0xca, v166
	v_add_u32_e32 v180, 0xea, v166
	v_add_u32_e32 v181, 0xcb, v166
	v_add_u32_e32 v182, 0xeb, v166
	v_add_u32_e32 v183, 0xd0, v166
	v_add_u32_e32 v184, 0xf0, v166
	v_add_u32_e32 v185, 0xd1, v166
	v_add_u32_e32 v186, 0xf1, v166
	v_add_u32_e32 v187, 0xd2, v166
	v_add_u32_e32 v188, 0xf2, v166
	v_add_u32_e32 v189, 0xd3, v166
	v_add_u32_e32 v190, 0xf3, v166
	v_add_u32_e32 v191, 0xd8, v166
	v_add_u32_e32 v192, 0xf8, v166
	v_add_u32_e32 v193, 0xd9, v166
	v_add_u32_e32 v194, 0xf9, v166
	v_add_u32_e32 v195, 0xda, v166
	v_add_u32_e32 v196, 0xfa, v166
	v_add_u32_e32 v197, 0xdb, v166
	v_add_u32_e32 v166, 0xfb, v166
	v_cmp_lt_i32_e64 s[44:45], v167, v163
	v_cmp_lt_i32_e64 s[6:7], v168, v163
	v_cmp_lt_i32_e64 s[68:69], v169, v163
	v_cmp_lt_i32_e64 s[0:1], v170, v163
	v_cmp_lt_i32_e64 s[72:73], v171, v163
	v_cmp_lt_i32_e64 s[40:41], v172, v163
	v_cmp_lt_i32_e64 s[76:77], v173, v163
	v_cmp_lt_i32_e64 s[42:43], v174, v163
	v_cmp_lt_i32_e64 s[78:79], v175, v163
	v_cmp_lt_i32_e64 s[48:49], v176, v163
	v_cmp_lt_i32_e64 s[80:81], v177, v163
	v_cmp_lt_i32_e64 s[50:51], v178, v163
	v_cmp_lt_i32_e64 s[82:83], v179, v163
	v_cmp_lt_i32_e64 s[52:53], v180, v163
	v_cmp_lt_i32_e64 s[84:85], v181, v163
	v_cmp_lt_i32_e64 s[54:55], v182, v163
	v_cmp_lt_i32_e64 s[88:89], v183, v163
	v_cmp_lt_i32_e64 s[58:59], v184, v163
	v_cmp_lt_i32_e64 s[90:91], v185, v163
	v_cmp_lt_i32_e64 s[60:61], v186, v163
	v_cmp_lt_i32_e64 s[92:93], v187, v163
	v_cmp_lt_i32_e64 s[62:63], v188, v163
	v_cmp_lt_i32_e64 s[94:95], v189, v163
	v_cmp_lt_i32_e64 s[64:65], v190, v163
	v_cmp_lt_i32_e64 s[96:97], v191, v163
	v_cmp_lt_i32_e64 s[66:67], v192, v163
	v_cmp_lt_i32_e64 s[4:5], v193, v163
	v_cmp_lt_i32_e64 s[70:71], v194, v163
	v_cmp_lt_i32_e32 vcc, v195, v163
	v_cmp_lt_i32_e64 s[74:75], v196, v163
	v_cmp_lt_i32_e64 s[86:87], v197, v163
	v_cmp_lt_i32_e64 s[56:57], v166, v163
	s_nop 1
	s_or_b64 vcc, s[86:87], vcc
	v_cndmask_b32_e32 v78, 0, v78, vcc
	s_or_b64 vcc, vcc, s[4:5]
	v_cndmask_b32_e32 v75, 0, v75, vcc
	s_or_b64 vcc, vcc, s[96:97]
	v_cndmask_b32_e32 v74, 0, v74, vcc
	s_or_b64 vcc, vcc, s[94:95]
	v_cndmask_b32_e32 v71, 0, v71, vcc
	s_or_b64 vcc, vcc, s[92:93]
	v_cndmask_b32_e32 v70, 0, v70, vcc
	s_or_b64 vcc, vcc, s[90:91]
	v_cndmask_b32_e32 v67, 0, v67, vcc
	s_or_b64 vcc, vcc, s[88:89]
	v_cndmask_b32_e32 v66, 0, v66, vcc
	s_or_b64 vcc, vcc, s[84:85]
	v_cndmask_b32_e32 v63, 0, v63, vcc
	s_or_b64 vcc, vcc, s[82:83]
	v_cndmask_b32_e32 v62, 0, v62, vcc
	s_or_b64 vcc, vcc, s[80:81]
	v_cndmask_b32_e32 v59, 0, v59, vcc
	s_or_b64 vcc, vcc, s[78:79]
	v_cndmask_b32_e32 v58, 0, v58, vcc
	s_or_b64 vcc, vcc, s[76:77]
	v_cndmask_b32_e32 v55, 0, v55, vcc
	s_or_b64 vcc, vcc, s[72:73]
	v_cndmask_b32_e32 v54, 0, v54, vcc
	s_or_b64 vcc, vcc, s[68:69]
	v_cndmask_b32_e32 v1, 0, v1, vcc
	s_or_b64 vcc, vcc, s[44:45]
	v_cndmask_b32_e32 v2, 0, v2, vcc
	s_or_b64 vcc, s[56:57], s[74:75]
	v_cndmask_b32_e32 v80, 0, v80, vcc
	s_or_b64 vcc, vcc, s[70:71]
	v_cndmask_b32_e32 v77, 0, v77, vcc
	s_or_b64 vcc, vcc, s[66:67]
	v_cndmask_b32_e32 v76, 0, v76, vcc
	s_or_b64 vcc, vcc, s[64:65]
	v_cndmask_b32_e32 v73, 0, v73, vcc
	s_or_b64 vcc, vcc, s[62:63]
	v_cndmask_b32_e32 v72, 0, v72, vcc
	s_or_b64 vcc, vcc, s[60:61]
	v_cndmask_b32_e32 v69, 0, v69, vcc
	s_or_b64 vcc, vcc, s[58:59]
	v_cndmask_b32_e32 v68, 0, v68, vcc
	s_or_b64 vcc, vcc, s[54:55]
	v_cndmask_b32_e32 v65, 0, v65, vcc
	s_or_b64 vcc, vcc, s[52:53]
	v_cndmask_b32_e32 v64, 0, v64, vcc
	s_or_b64 vcc, vcc, s[50:51]
	v_cndmask_b32_e32 v61, 0, v61, vcc
	s_or_b64 vcc, vcc, s[48:49]
	v_cndmask_b32_e32 v60, 0, v60, vcc
	s_or_b64 vcc, vcc, s[42:43]
	v_cndmask_b32_e32 v57, 0, v57, vcc
	s_or_b64 vcc, vcc, s[40:41]
	v_cndmask_b32_e32 v56, 0, v56, vcc
	s_or_b64 vcc, vcc, s[0:1]
	v_cndmask_b32_e32 v53, 0, v53, vcc
	s_or_b64 vcc, vcc, s[6:7]
	v_cndmask_b32_e64 v79, 0, v79, s[86:87]
	v_cndmask_b32_e32 v52, 0, v52, vcc
	v_cndmask_b32_e64 v81, 0, v81, s[56:57]
